# h1_hoist
# baseline (speedup 1.0000x reference)
.LBB1_14:
	v_lshl_add_u64 v[208:209], v[204:205], 0, s[4:5]
	v_lshl_add_u64 v[248:249], v[208:209], 0, s[14:15]
	s_add_i32 s49, s48, s38
	s_mov_b32 s50, m0
	s_mov_b32 m0, s49
	s_nop 0
	global_load_lds_dwordx4 v[248:249], off
	s_mov_b32 m0, s50
	v_lshl_add_u64 v[248:249], v[208:209], 0, s[16:17]
	v_lshl_add_u64 v[210:211], v[206:207], 0, s[4:5]
	s_addk_i32 s49, 0x1000
	s_mov_b32 s50, m0
	s_mov_b32 m0, s49
	s_nop 0
	global_load_lds_dwordx4 v[248:249], off
	s_mov_b32 m0, s50
	v_lshl_add_u64 v[248:249], v[210:211], 0, s[18:19]
	s_add_i32 s49, s45, s39
	s_mov_b32 s50, m0
	s_mov_b32 m0, s49
	s_nop 0
	global_load_lds_dwordx4 v[248:249], off
	s_mov_b32 m0, s50
	v_lshl_add_u64 v[248:249], v[210:211], 0, s[20:21]
	s_addk_i32 s49, 0x1000
	s_mov_b32 s50, m0
	s_mov_b32 m0, s49
	s_nop 0
	global_load_lds_dwordx4 v[248:249], off
	s_mov_b32 m0, s50
	v_add_u32_e32 v203, s30, v240
	ds_read_b64_tr_b16 v[196:197], v203 offset:24576
	ds_read_b64_tr_b16 v[198:199], v203 offset:25088
	s_waitcnt lgkmcnt(9)
	v_mfma_f32_32x32x16_f16 v[112:127], v[192:195], v[148:151], v[48:63]
	v_cvt_pk_f16_f32 v156, v80, v81
	v_cvt_pk_f16_f32 v157, v82, v83
	s_nop 0
	ds_read_b64_tr_b16 v[192:193], v203 offset:28672
	ds_read_b64_tr_b16 v[194:195], v203 offset:29184
	s_waitcnt lgkmcnt(10)
	v_mfma_f32_32x32x16_f16 v[96:111], v[188:191], v[148:151], v[48:63]
	v_cvt_pk_f16_f32 v158, v84, v85
	v_cvt_pk_f16_f32 v159, v86, v87
	s_nop 0
	ds_read_b64_tr_b16 v[188:189], v203 offset:25600
	ds_read_b64_tr_b16 v[190:191], v203 offset:26112
	s_waitcnt lgkmcnt(11)
	v_mfma_f32_32x32x16_f16 v[112:127], v[184:187], v[140:143], v[112:127]
	v_cvt_pk_f16_f32 v160, v88, v89
	v_cvt_pk_f16_f32 v161, v90, v91
	s_nop 0
	ds_read_b64_tr_b16 v[88:89], v203 offset:29696
	ds_read_b64_tr_b16 v[90:91], v203 offset:30208
	s_waitcnt lgkmcnt(12)
	v_mfma_f32_32x32x16_f16 v[96:111], v[176:179], v[140:143], v[96:111]
	v_cvt_pk_f16_f32 v162, v92, v93
	v_cvt_pk_f16_f32 v163, v94, v95
	s_nop 0
	ds_read_b64_tr_b16 v[84:85], v203 offset:26624
	ds_read_b64_tr_b16 v[86:87], v203 offset:27136
	s_waitcnt lgkmcnt(13)
	v_mfma_f32_32x32x16_f16 v[112:127], v[180:183], v[136:139], v[112:127]
	v_cvt_pk_f16_f32 v152, v64, v65
	v_cvt_pk_f16_f32 v153, v66, v67
	s_nop 0
	ds_read_b64_tr_b16 v[80:81], v203 offset:30720
	ds_read_b64_tr_b16 v[82:83], v203 offset:31232
	s_waitcnt lgkmcnt(14)
	v_mfma_f32_32x32x16_f16 v[96:111], v[172:175], v[136:139], v[96:111]
	v_cvt_pk_f16_f32 v154, v68, v69
	v_cvt_pk_f16_f32 v155, v70, v71
	s_nop 0
	ds_read_b64_tr_b16 v[68:69], v203 offset:27648
	ds_read_b64_tr_b16 v[70:71], v203 offset:28160
	s_waitcnt lgkmcnt(14)
	v_mfma_f32_32x32x16_f16 v[112:127], v[168:171], v[132:135], v[112:127]
	v_cvt_pk_f16_f32 v144, v72, v73
	v_cvt_pk_f16_f32 v145, v74, v75
	s_nop 0
	ds_read_b64_tr_b16 v[64:65], v203 offset:31744
	ds_read_b64_tr_b16 v[66:67], v203 offset:32256
	v_mfma_f32_32x32x16_f16 v[96:111], v[164:167], v[132:135], v[96:111]
	v_cvt_pk_f16_f32 v146, v76, v77
	v_cvt_pk_f16_f32 v147, v78, v79
	s_nop 0
	s_nop 7
	s_nop 5
	v_max_f32_e32 v72, v113, v113
	v_max_f32_e32 v73, v112, v112
	v_max_f32_e32 v72, v73, v72
	v_max3_f32 v73, v114, v115, v97
	v_max3_f32 v72, v72, v96, v98
	v_max3_f32 v72, v72, v99, v116
	v_max3_f32 v73, v73, v118, v119
	v_max3_f32 v72, v72, v117, v100
	v_max3_f32 v73, v73, v102, v103
	v_max3_f32 v72, v72, v101, v120
	v_max3_f32 v73, v73, v122, v123
	v_max3_f32 v72, v72, v121, v104
	v_max3_f32 v73, v73, v106, v107
	v_max3_f32 v72, v72, v105, v124
	v_max3_f32 v73, v73, v126, v127
	v_max3_f32 v72, v72, v125, v108
	v_max3_f32 v73, v73, v110, v111
	v_max3_f32 v72, v72, v109, v73
	v_mov_b32_e32 v73, v72
	s_nop 1
	v_permlane32_swap_b32_e32 v72, v73
	v_max_f32_e32 v73, v73, v73
	v_max_f32_e32 v72, v72, v72
	v_max_f32_e32 v72, v72, v73
	v_cmp_lt_f32_e32 vcc, s47, v72
	s_cmp_lg_u64 vcc, 0
	s_cselect_b64 s[30:31], -1, 0
	s_cbranch_vccnz .LBB1_22

.LBB1_17:
	s_add_i32 s30, s45, 0x2000
	s_cmpk_lg_i32 s45, 0x4000
	s_cselect_b32 s41, s30, 0
	v_lshl_add_u64 v[248:249], v[208:209], 0, s[22:23]
	s_add_i32 s49, s45, s38
	s_mov_b32 s50, m0
	s_mov_b32 m0, s49
	s_nop 0
	global_load_lds_dwordx4 v[248:249], off
	s_mov_b32 m0, s50
	v_lshl_add_u64 v[248:249], v[208:209], 0, s[24:25]
	s_addk_i32 s49, 0x1000
	s_mov_b32 s50, m0
	s_mov_b32 m0, s49
	s_nop 0
	global_load_lds_dwordx4 v[248:249], off
	s_mov_b32 m0, s50
	v_lshl_add_u64 v[248:249], v[210:211], 0, s[26:27]
	s_add_i32 s49, s41, s39
	s_mov_b32 s50, m0
	s_mov_b32 m0, s49
	s_nop 0
	global_load_lds_dwordx4 v[248:249], off
	s_mov_b32 m0, s50
	v_lshl_add_u64 v[248:249], v[210:211], 0, s[28:29]
	s_addk_i32 s49, 0x1000
	s_mov_b32 s50, m0
	s_mov_b32 m0, s49
	s_nop 0
	global_load_lds_dwordx4 v[248:249], off
	s_mov_b32 m0, s50
	v_add_u32_e32 v203, s48, v240
	ds_read_b64_tr_b16 v[196:197], v203 offset:24576
	ds_read_b64_tr_b16 v[198:199], v203 offset:25088
	s_waitcnt lgkmcnt(9)
	v_mfma_f32_32x32x16_f16 v[80:95], v[72:75], v[148:151], v[48:63]
	v_cvt_pk_f16_f32 v156, v112, v113
	v_cvt_pk_f16_f32 v157, v114, v115
	s_nop 0
	ds_read_b64_tr_b16 v[192:193], v203 offset:28672
	ds_read_b64_tr_b16 v[194:195], v203 offset:29184
	s_waitcnt lgkmcnt(10)
	v_mfma_f32_32x32x16_f16 v[64:79], v[180:183], v[148:151], v[48:63]
	v_cvt_pk_f16_f32 v158, v116, v117
	v_cvt_pk_f16_f32 v159, v118, v119
	s_nop 0
	ds_read_b64_tr_b16 v[180:181], v203 offset:25600
	ds_read_b64_tr_b16 v[182:183], v203 offset:26112
	s_waitcnt lgkmcnt(11)
	v_mfma_f32_32x32x16_f16 v[80:95], v[184:187], v[140:143], v[80:95]
	v_cvt_pk_f16_f32 v160, v120, v121
	v_cvt_pk_f16_f32 v161, v122, v123
	s_nop 0
	ds_read_b64_tr_b16 v[120:121], v203 offset:29696
	ds_read_b64_tr_b16 v[122:123], v203 offset:30208
	s_waitcnt lgkmcnt(12)
	v_mfma_f32_32x32x16_f16 v[64:79], v[168:171], v[140:143], v[64:79]
	v_cvt_pk_f16_f32 v162, v124, v125
	v_cvt_pk_f16_f32 v163, v126, v127
	s_nop 0
	ds_read_b64_tr_b16 v[116:117], v203 offset:26624
	ds_read_b64_tr_b16 v[118:119], v203 offset:27136
	s_waitcnt lgkmcnt(13)
	v_mfma_f32_32x32x16_f16 v[80:95], v[188:191], v[136:139], v[80:95]
	v_cvt_pk_f16_f32 v152, v96, v97
	v_cvt_pk_f16_f32 v153, v98, v99
	s_nop 0
	ds_read_b64_tr_b16 v[112:113], v203 offset:30720
	ds_read_b64_tr_b16 v[114:115], v203 offset:31232
	s_waitcnt lgkmcnt(14)
	v_mfma_f32_32x32x16_f16 v[64:79], v[172:175], v[136:139], v[64:79]
	v_cvt_pk_f16_f32 v154, v100, v101
	v_cvt_pk_f16_f32 v155, v102, v103
	s_nop 0
	ds_read_b64_tr_b16 v[100:101], v203 offset:27648
	ds_read_b64_tr_b16 v[102:103], v203 offset:28160
	s_waitcnt lgkmcnt(14)
	v_mfma_f32_32x32x16_f16 v[80:95], v[176:179], v[132:135], v[80:95]
	v_cvt_pk_f16_f32 v144, v104, v105
	v_cvt_pk_f16_f32 v145, v106, v107
	s_nop 0
	ds_read_b64_tr_b16 v[96:97], v203 offset:31744
	ds_read_b64_tr_b16 v[98:99], v203 offset:32256
	v_mfma_f32_32x32x16_f16 v[64:79], v[164:167], v[132:135], v[64:79]
	v_cvt_pk_f16_f32 v146, v108, v109
	v_cvt_pk_f16_f32 v147, v110, v111
	s_nop 0
	s_nop 7
	s_nop 5
	v_max_f32_e32 v104, v81, v81
	v_max_f32_e32 v105, v80, v80
	v_max_f32_e32 v104, v105, v104
	v_max3_f32 v105, v82, v83, v65
	v_max3_f32 v104, v104, v64, v66
	v_max3_f32 v104, v104, v67, v84
	v_max3_f32 v105, v105, v86, v87
	v_max3_f32 v104, v104, v85, v68
	v_max3_f32 v105, v105, v70, v71
	v_max3_f32 v104, v104, v69, v88
	v_max3_f32 v105, v105, v90, v91
	v_max3_f32 v104, v104, v89, v72
	v_max3_f32 v105, v105, v74, v75
	v_max3_f32 v104, v104, v73, v92
	v_max3_f32 v105, v105, v94, v95
	v_max3_f32 v104, v104, v93, v76
	v_max3_f32 v105, v105, v78, v79
	v_max3_f32 v104, v104, v77, v105
	v_mov_b32_e32 v105, v104
	s_nop 1
	v_permlane32_swap_b32_e32 v104, v105
	v_max_f32_e32 v105, v105, v105
	v_max_f32_e32 v104, v104, v104
	v_max_f32_e32 v104, v104, v105
	v_cmp_lt_f32_e32 vcc, s47, v104
	s_cmp_lg_u64 vcc, 0
	s_cselect_b64 s[30:31], -1, 0
	s_cbranch_vccnz .LBB1_25

	.amdhsa_kernel _Z10attn64_fwdPKDF16_S0_S0_PDF16_
		.amdhsa_group_segment_fixed_size 0
		.amdhsa_private_segment_fixed_size 0
		.amdhsa_kernarg_size 32
		.amdhsa_user_sgpr_count 2
		.amdhsa_user_sgpr_dispatch_ptr 0
		.amdhsa_user_sgpr_queue_ptr 0
		.amdhsa_user_sgpr_kernarg_segment_ptr 1
		.amdhsa_user_sgpr_dispatch_id 0
		.amdhsa_user_sgpr_kernarg_preload_length 0
		.amdhsa_user_sgpr_kernarg_preload_offset 0
		.amdhsa_user_sgpr_private_segment_size 0
		.amdhsa_uses_dynamic_stack 0
		.amdhsa_enable_private_segment 0
		.amdhsa_system_sgpr_workgroup_id_x 1
		.amdhsa_system_sgpr_workgroup_id_y 0
		.amdhsa_system_sgpr_workgroup_id_z 0
		.amdhsa_system_sgpr_workgroup_info 0
		.amdhsa_system_vgpr_workitem_id 0
		.amdhsa_next_free_vgpr 250
		.amdhsa_next_free_sgpr 51
		.amdhsa_accum_offset 252
		.amdhsa_reserve_vcc 1
		.amdhsa_float_round_mode_32 0
		.amdhsa_float_round_mode_16_64 0
		.amdhsa_float_denorm_mode_32 3
		.amdhsa_float_denorm_mode_16_64 3
		.amdhsa_dx10_clamp 1
		.amdhsa_ieee_mode 1
		.amdhsa_fp16_overflow 0
		.amdhsa_tg_split 0
		.amdhsa_exception_fp_ieee_invalid_op 0
		.amdhsa_exception_fp_denorm_src 0
		.amdhsa_exception_fp_ieee_div_zero 0
		.amdhsa_exception_fp_ieee_overflow 0
		.amdhsa_exception_fp_ieee_underflow 0
		.amdhsa_exception_fp_ieee_inexact 0
		.amdhsa_exception_int_div_zero 0
	.end_amdhsa_kernel

amdhsa.kernels:
  - .agpr_count:     0
    .args:
      - .address_space:  global
        .offset:         0
        .size:           8
        .value_kind:     global_buffer
      - .address_space:  global
        .offset:         8
        .size:           8
        .value_kind:     global_buffer
      - .address_space:  global
        .offset:         16
        .size:           8
        .value_kind:     global_buffer
      - .address_space:  global
        .offset:         24
        .size:           8
        .value_kind:     global_buffer
      - .address_space:  global
        .offset:         32
        .size:           8
        .value_kind:     global_buffer
      - .actual_access:  write_only
        .address_space:  global
        .offset:         40
        .size:           8
        .value_kind:     global_buffer
      - .actual_access:  write_only
        .address_space:  global
        .offset:         48
        .size:           8
        .value_kind:     global_buffer
      - .actual_access:  write_only
        .address_space:  global
        .offset:         56
        .size:           8
        .value_kind:     global_buffer
      - .actual_access:  write_only
        .address_space:  global
        .offset:         64
        .size:           8
        .value_kind:     global_buffer
    .group_segment_fixed_size: 0
    .kernarg_segment_align: 8
    .kernarg_segment_size: 72
    .language:       OpenCL C
    .language_version:
      - 2
      - 0
    .max_flat_workgroup_size: 256
    .name:           _Z11prep_kernelPKfS0_S0_S0_S0_PDF16_S1_S1_P15HIP_vector_typeIfLj2EE
    .private_segment_fixed_size: 0
    .sgpr_count:     38
    .sgpr_spill_count: 0
    .symbol:         _Z11prep_kernelPKfS0_S0_S0_S0_PDF16_S1_S1_P15HIP_vector_typeIfLj2EE.kd
    .uniform_work_group_size: 1
    .uses_dynamic_stack: false
    .vgpr_count:     44
    .vgpr_spill_count: 0
    .wavefront_size: 64
  - .agpr_count:     0
    .args:
      - .address_space:  global
        .offset:         0
        .size:           8
        .value_kind:     global_buffer
      - .address_space:  global
        .offset:         8
        .size:           8
        .value_kind:     global_buffer
      - .address_space:  global
        .offset:         16
        .size:           8
        .value_kind:     global_buffer
      - .address_space:  global
        .offset:         24
        .size:           8
        .value_kind:     global_buffer
    .group_segment_fixed_size: 0
    .kernarg_segment_align: 8
    .kernarg_segment_size: 32
    .language:       OpenCL C
    .language_version:
      - 2
      - 0
    .max_flat_workgroup_size: 256
    .name:           _Z10attn64_fwdPKDF16_S0_S0_PDF16_
    .private_segment_fixed_size: 0
    .sgpr_count:     57
    .sgpr_spill_count: 0
    .symbol:         _Z10attn64_fwdPKDF16_S0_S0_PDF16_.kd
    .uniform_work_group_size: 1
    .uses_dynamic_stack: false
    .vgpr_count:     250
    .vgpr_spill_count: 0
    .wavefront_size: 64
  - .agpr_count:     0
    .args:
      - .address_space:  global
        .offset:         0
        .size:           8
        .value_kind:     global_buffer
      - .address_space:  global
        .offset:         8
        .size:           8
        .value_kind:     global_buffer
      - .actual_access:  read_only
        .address_space:  global
        .offset:         16
        .size:           8
        .value_kind:     global_buffer
      - .actual_access:  write_only
        .address_space:  global
        .offset:         24
        .size:           8
        .value_kind:     global_buffer
      - .actual_access:  write_only
        .address_space:  global
        .offset:         32
        .size:           8
        .value_kind:     global_buffer
      - .actual_access:  write_only
        .address_space:  global
        .offset:         40
        .size:           8
        .value_kind:     global_buffer
      - .actual_access:  read_only
        .address_space:  global
        .offset:         48
        .size:           8
        .value_kind:     global_buffer
    .group_segment_fixed_size: 0
    .kernarg_segment_align: 8
    .kernarg_segment_size: 56
    .language:       OpenCL C
    .language_version:
      - 2
      - 0
    .max_flat_workgroup_size: 768
    .name:           _Z11gemm_kernelILi0ELi6ELi4ELi5EEvPKDF16_S1_PK15HIP_vector_typeIfLj4EEPDF16_S6_S6_Pf
    .private_segment_fixed_size: 0
    .sgpr_count:     56
    .sgpr_spill_count: 0
    .symbol:         _Z11gemm_kernelILi0ELi6ELi4ELi5EEvPKDF16_S1_PK15HIP_vector_typeIfLj4EEPDF16_S6_S6_Pf.kd
    .uniform_work_group_size: 1
    .uses_dynamic_stack: false
    .vgpr_count:     168
    .vgpr_spill_count: 0
    .wavefront_size: 64
  - .agpr_count:     0
    .args:
      - .address_space:  global
        .offset:         0
        .size:           8
        .value_kind:     global_buffer
      - .address_space:  global
        .offset:         8
        .size:           8
        .value_kind:     global_buffer
      - .actual_access:  read_only
        .address_space:  global
        .offset:         16
        .size:           8
        .value_kind:     global_buffer
      - .actual_access:  read_only
        .address_space:  global
        .offset:         24
        .size:           8
        .value_kind:     global_buffer
      - .actual_access:  read_only
        .address_space:  global
        .offset:         32
        .size:           8
        .value_kind:     global_buffer
      - .actual_access:  read_only
        .address_space:  global
        .offset:         40
        .size:           8
        .value_kind:     global_buffer
      - .actual_access:  write_only
        .address_space:  global
        .offset:         48
        .size:           8
        .value_kind:     global_buffer
    .group_segment_fixed_size: 0
    .kernarg_segment_align: 8
    .kernarg_segment_size: 56
    .language:       OpenCL C
    .language_version:
      - 2
      - 0
    .max_flat_workgroup_size: 768
    .name:           _Z11gemm_kernelILi1ELi4ELi2ELi5EEvPKDF16_S1_PK15HIP_vector_typeIfLj4EEPDF16_S6_S6_Pf
    .private_segment_fixed_size: 0
    .sgpr_count:     19
    .sgpr_spill_count: 0
    .symbol:         _Z11gemm_kernelILi1ELi4ELi2ELi5EEvPKDF16_S1_PK15HIP_vector_typeIfLj4EEPDF16_S6_S6_Pf.kd
    .uniform_work_group_size: 1
    .uses_dynamic_stack: false
    .vgpr_count:     62
    .vgpr_spill_count: 0
    .wavefront_size: 64
